# speedup vs baseline: 1.0149x; 1.0149x over previous
.LBB2_3:
	s_lshl_b32 s63, s53, 1
	s_add_i32 s61, s63, 2
	s_sub_i32 s2, s61, s40
	s_lshl_b32 s60, s53, 7
	s_min_i32 s62, s33, s2
	s_cmp_eq_u32 s55, 0
	s_cselect_b32 s79, 0, s62
	s_cmp_lt_i32 s2, 1
	s_waitcnt vmcnt(0)
	s_barrier
	s_cbranch_scc1 .LBB2_21
	s_add_i32 s63, s63, s55
	v_lshl_or_b32 v11, s63, 6, v83
	v_add_u32_e32 v10, s60, v82
	v_or_b32_e32 v12, 2, v11
	v_cmp_gt_i32_e64 s[6:7], v12, v10
	v_or_b32_e32 v12, 3, v11
	v_cmp_gt_i32_e64 s[8:9], v12, v10
	v_or_b32_e32 v12, 16, v11
	v_cmp_gt_i32_e64 s[10:11], v12, v10
	v_or_b32_e32 v12, 17, v11
	v_cmp_gt_i32_e64 s[12:13], v12, v10
	v_or_b32_e32 v12, 18, v11
	v_cmp_gt_i32_e64 s[14:15], v12, v10
	v_or_b32_e32 v12, 19, v11
	v_cmp_gt_i32_e64 s[16:17], v12, v10
	v_or_b32_e32 v12, 32, v11
	v_cmp_gt_i32_e64 s[18:19], v12, v10
	v_or_b32_e32 v12, 33, v11
	v_cmp_gt_i32_e64 s[20:21], v12, v10
	v_or_b32_e32 v12, 34, v11
	v_cmp_gt_i32_e64 s[22:23], v12, v10
	v_or_b32_e32 v12, 35, v11
	v_cmp_gt_i32_e64 s[24:25], v12, v10
	v_or_b32_e32 v12, 48, v11
	s_sub_i32 s37, s56, s40
	v_cmp_gt_i32_e64 s[26:27], v12, v10
	v_or_b32_e32 v12, 49, v11
	s_min_i32 s37, s33, s37
	v_cmp_gt_i32_e64 s[2:3], v11, v10
	v_cmp_lt_i32_e64 s[4:5], v11, v10
	v_cmp_gt_i32_e64 s[28:29], v12, v10
	v_or_b32_e32 v12, 50, v11
	v_or_b32_e32 v11, 51, v11
	s_max_i32 s37, s37, 1
	s_lshl_b64 s[38:39], s[40:41], 13
	v_mov_b32_e32 v67, 0
	v_cmp_gt_i32_e64 s[30:31], v12, v10
	v_cmp_gt_i32_e64 s[34:35], v11, v10
	s_mov_b32 s64, 1
	s_sub_i32 s65, 0, s37
	s_add_i32 s66, s40, s57
	s_add_u32 s68, s70, s38
	s_addc_u32 s69, s71, s39
	s_add_u32 s74, s72, s38
	s_addc_u32 s75, s73, s39
	v_mov_b32_e32 v14, v51
	v_mov_b32_e32 v15, v51
	v_mov_b32_e32 v16, v51
	v_mov_b32_e32 v17, v51
	s_mov_b64 s[38:39], -1
	v_mov_b32_e32 v30, 0
	v_mov_b32_e32 v31, v67
	v_mov_b32_e32 v32, v67
	v_mov_b32_e32 v33, v67
	v_mov_b32_e32 v26, 0
	v_mov_b32_e32 v27, v67
	v_mov_b32_e32 v28, v67
	v_mov_b32_e32 v29, v67
	v_mov_b32_e32 v22, v67
	v_mov_b32_e32 v23, v67
	v_mov_b32_e32 v24, v67
	v_mov_b32_e32 v25, v67
	v_mov_b32_e32 v18, v67
	v_mov_b32_e32 v19, v67
	v_mov_b32_e32 v20, v67
	v_mov_b32_e32 v21, v67
	v_mov_b32_e32 v10, v67
	v_mov_b32_e32 v11, v67
	v_mov_b32_e32 v12, v67
	v_mov_b32_e32 v13, v67
	s_mov_b32 s37, 0
	s_mov_b32 s80, 0
	s_mov_b32 s81, 0
	s_mov_b32 s48, s40
	v_mov_b32_e32 v114, v57
	v_mov_b32_e32 v115, v81
	v_mov_b32_e32 v120, v57
	v_mov_b32_e32 v121, v81
	s_cmp_gt_u32 s48, s63
	s_branch .Lattn_after_rdv
.LBB2_5:
	ds_read_b128 v[102:105], v120 offset:8192
	ds_read_b128 v[106:109], v120 offset:10240
	ds_read_b128 v[110:113], v120 offset:12288
	v_exp_f32_e32 v69, v46
	v_exp_f32_e32 v71, v47
	v_exp_f32_e32 v73, v48
	v_exp_f32_e32 v75, v49
	ds_read_b128 v[46:49], v120 offset:14336
	v_exp_f32_e32 v42, v42
	v_exp_f32_e32 v43, v43
	v_exp_f32_e32 v44, v44
	v_exp_f32_e32 v45, v45
	v_cvt_pk_f16_f32 v76, v69, v71
	v_cvt_pk_f16_f32 v77, v73, v75
	v_cvt_pk_f16_f32 v78, v42, v43
	v_cvt_pk_f16_f32 v79, v44, v45
	ds_read_b128 v[42:45], v121 offset:8192
	v_exp_f32_e32 v38, v38
	v_exp_f32_e32 v39, v39
	s_waitcnt lgkmcnt(4)
	v_mfma_f32_16x16x32_f16 v[26:29], v[102:105], v[76:79], v[26:29]
	v_exp_f32_e32 v40, v40
	v_exp_f32_e32 v41, v41
	s_waitcnt lgkmcnt(3)
	v_mfma_f32_16x16x32_f16 v[22:25], v[106:109], v[76:79], v[22:25]
	ds_read_b128 v[102:105], v121 offset:10240
	v_exp_f32_e32 v34, v34
	v_exp_f32_e32 v35, v35
	s_waitcnt lgkmcnt(3)
	v_mfma_f32_16x16x32_f16 v[18:21], v[110:113], v[76:79], v[18:21]
	ds_read_b128 v[106:109], v121 offset:12288
	v_exp_f32_e32 v36, v36
	v_exp_f32_e32 v37, v37
	s_waitcnt lgkmcnt(3)
	v_mfma_f32_16x16x32_f16 v[10:13], v[46:49], v[76:79], v[10:13]
	ds_read_b128 v[110:113], v121 offset:14336
	v_mfma_f32_16x16x32_f16 v[14:17], v[116:119], v[76:79], v[14:17]
	v_cvt_pk_f16_f32 v37, v36, v37
	v_cvt_pk_f16_f32 v36, v34, v35
	v_cvt_pk_f16_f32 v35, v40, v41
	v_cvt_pk_f16_f32 v34, v38, v39
	s_mov_b64 s[38:39], 0
	s_waitcnt lgkmcnt(3)
	v_mfma_f32_16x16x32_f16 v[26:29], v[42:45], v[34:37], v[26:29]
	s_waitcnt lgkmcnt(2)
	v_mfma_f32_16x16x32_f16 v[22:25], v[102:105], v[34:37], v[22:25]
	s_waitcnt lgkmcnt(1)
	v_mfma_f32_16x16x32_f16 v[18:21], v[106:109], v[34:37], v[18:21]
	s_waitcnt lgkmcnt(0)
	v_mfma_f32_16x16x32_f16 v[10:13], v[110:113], v[34:37], v[10:13]
	v_mfma_f32_16x16x32_f16 v[14:17], v[116:119], v[34:37], v[14:17]
	s_cmp_eq_u32 s55, 0
	s_cbranch_scc1 .LBB2_6
	s_mov_b32 s80, 0
	s_cmp_eq_u32 s81, 0
	s_cbranch_scc1 .Lattn_A
	s_branch .Lattn_post
.LBB2_6:
	s_add_i32 s64, s64, 1
	s_add_u32 s68, s68, 0x2000
	s_addc_u32 s69, s69, 0
	s_add_u32 s74, s74, 0x2000
	s_addc_u32 s75, s75, 0
	s_add_i32 s82, s65, s64
	s_cmp_eq_u32 s82, 1
	s_cbranch_scc1 .Lattn_last_step
	v_mov_b32_e32 v120, v114
	v_mov_b32_e32 v121, v115
	s_add_i32 s37, s37, 0x4000
	s_cmp_eq_u32 s37, 0xc000
	s_cselect_b32 s37, 0, s37
	s_add_i32 s48, s40, s64
	s_add_i32 s48, s48, -1
	v_or_b32_e32 v114, s37, v57
	v_or_b32_e32 v115, s37, v81
	s_cmp_eq_u32 s55, 0
	s_cbranch_scc0 .Lattn_pre_done
	v_mov_b32_e32 v120, v114
	v_mov_b32_e32 v121, v115

.Lattn_after_rdv:
	s_cbranch_scc1 .Lattn_skip_tile
	s_cmp_lt_i32 s64, s79
	s_cbranch_scc1 .Lattn_do_dma
.Lattn_no_dma:
	s_cmp_eq_u32 s80, 0
	s_cbranch_scc0 .LBB2_5
.Lattn_A:
	ds_read_b128 v[34:37], v114
	ds_read_b128 v[38:41], v114 offset:2048
	ds_read_b128 v[42:45], v114 offset:4096
	ds_read_b128 v[110:113], v115 offset:2048
	ds_read_b128 v[46:49], v114 offset:6144
	s_add_i32 s48, s66, s64
	s_cmp_lg_u32 s48, 1
	s_waitcnt lgkmcnt(4)
	v_mfma_f32_16x16x32_f16 v[34:37], v[34:37], v[6:9], v[30:33]
	s_waitcnt lgkmcnt(2)
	v_mfma_f32_16x16x32_f16 v[102:105], v[42:45], v[6:9], v[30:33]
	ds_read_b128 v[42:45], v115
	v_mfma_f32_16x16x32_f16 v[38:41], v[38:41], v[6:9], v[30:33]
	s_waitcnt lgkmcnt(1)
	v_mfma_f32_16x16x32_f16 v[106:109], v[46:49], v[6:9], v[30:33]
	s_waitcnt lgkmcnt(0)
	v_mfma_f32_16x16x32_f16 v[46:49], v[42:45], v[2:5], v[34:37]
	s_nop 2
	ds_read_b128 v[34:37], v115 offset:4096
	v_mfma_f32_16x16x32_f16 v[42:45], v[110:113], v[2:5], v[38:41]
	ds_read_b128 v[110:113], v115 offset:6144
	s_waitcnt lgkmcnt(0)
	v_mfma_f32_16x16x32_f16 v[38:41], v[34:37], v[2:5], v[102:105]
	v_mfma_f32_16x16x32_f16 v[34:37], v[110:113], v[2:5], v[106:109]
	s_cbranch_scc1 .LBB2_12
	v_cndmask_b32_e64 v69, v46, v100, s[2:3]
	v_cndmask_b32_e64 v46, v69, v46, s[4:5]
	v_cndmask_b32_e64 v47, v100, v47, s[4:5]
	v_cndmask_b32_e64 v48, v48, v100, s[6:7]
	v_cndmask_b32_e64 v49, v49, v100, s[8:9]
	v_cndmask_b32_e64 v42, v42, v100, s[10:11]
	v_cndmask_b32_e64 v43, v43, v100, s[12:13]
	v_cndmask_b32_e64 v44, v44, v100, s[14:15]
	v_cndmask_b32_e64 v45, v45, v100, s[16:17]
	v_cndmask_b32_e64 v38, v38, v100, s[18:19]
	v_cndmask_b32_e64 v39, v39, v100, s[20:21]
	v_cndmask_b32_e64 v40, v40, v100, s[22:23]
	v_cndmask_b32_e64 v41, v41, v100, s[24:25]
	v_cndmask_b32_e64 v34, v34, v100, s[26:27]
	v_cndmask_b32_e64 v35, v35, v100, s[28:29]
	v_cndmask_b32_e64 v36, v36, v100, s[30:31]
	v_cndmask_b32_e64 v37, v37, v100, s[34:35]

.Lattn_A_done:
	s_cmp_eq_u32 s55, 0
	s_cbranch_scc1 .LBB2_5
	s_mov_b32 s80, 1
	s_branch .LBB2_6

.Lattn_do_dma:
	s_add_i32 s48, s37, 0x4000
	s_cmp_eq_u32 s48, 0xc000
	s_cselect_b32 s48, 0, s48
	s_add_i32 s48, s78, s48
	s_mov_b32 m0, s48
	s_nop 0
	global_load_lds_dwordx4 v64, s[68:69]
	s_add_i32 m0, s48, 0x400
	s_nop 0
	global_load_lds_dwordx4 v65, s[68:69]
	s_add_i32 m0, s48, 0x2000
	s_nop 0
	global_load_lds_dwordx4 v64, s[74:75]
	s_add_i32 m0, s48, 0x2400
	s_nop 0
	global_load_lds_dwordx4 v65, s[74:75]
	s_branch .Lattn_no_dma
.Lattn_last_step:
	s_cmp_eq_u32 s80, 0
	s_cbranch_scc1 .Lattn_post
	v_mov_b32_e32 v120, v114
	v_mov_b32_e32 v121, v115
	s_mov_b32 s81, 1
	s_branch .LBB2_5
.Lattn_post:
	s_mov_b32 s81, 0
	s_waitcnt vmcnt(0) lgkmcnt(0)
	s_barrier

	.amdhsa_kernel _Z11attn_kernelPKDF16_S0_S0_PfPDF16_S1_
		.amdhsa_group_segment_fixed_size 65536
		.amdhsa_private_segment_fixed_size 0
		.amdhsa_kernarg_size 48
		.amdhsa_user_sgpr_count 2
		.amdhsa_user_sgpr_dispatch_ptr 0
		.amdhsa_user_sgpr_queue_ptr 0
		.amdhsa_user_sgpr_kernarg_segment_ptr 1
		.amdhsa_user_sgpr_dispatch_id 0
		.amdhsa_user_sgpr_kernarg_preload_length 0
		.amdhsa_user_sgpr_kernarg_preload_offset 0
		.amdhsa_user_sgpr_private_segment_size 0
		.amdhsa_uses_dynamic_stack 0
		.amdhsa_enable_private_segment 0
		.amdhsa_system_sgpr_workgroup_id_x 1
		.amdhsa_system_sgpr_workgroup_id_y 0
		.amdhsa_system_sgpr_workgroup_id_z 0
		.amdhsa_system_sgpr_workgroup_info 0
		.amdhsa_system_vgpr_workitem_id 0
		.amdhsa_next_free_vgpr 122
		.amdhsa_next_free_sgpr 96
		.amdhsa_accum_offset 124
		.amdhsa_reserve_vcc 1
		.amdhsa_float_round_mode_32 0
		.amdhsa_float_round_mode_16_64 0
		.amdhsa_float_denorm_mode_32 3
		.amdhsa_float_denorm_mode_16_64 3
		.amdhsa_dx10_clamp 1
		.amdhsa_ieee_mode 1
		.amdhsa_fp16_overflow 0
		.amdhsa_tg_split 0
		.amdhsa_exception_fp_ieee_invalid_op 0
		.amdhsa_exception_fp_denorm_src 0
		.amdhsa_exception_fp_ieee_div_zero 0
		.amdhsa_exception_fp_ieee_overflow 0
		.amdhsa_exception_fp_ieee_underflow 0
		.amdhsa_exception_fp_ieee_inexact 0
		.amdhsa_exception_int_div_zero 0
	.end_amdhsa_kernel

amdhsa.kernels:
  - .agpr_count:     0
    .args:
      - .actual_access:  read_only
        .address_space:  global
        .offset:         0
        .size:           8
        .value_kind:     global_buffer
      - .actual_access:  read_only
        .address_space:  global
        .offset:         8
        .size:           8
        .value_kind:     global_buffer
      - .actual_access:  read_only
        .address_space:  global
        .offset:         16
        .size:           8
        .value_kind:     global_buffer
      - .actual_access:  write_only
        .address_space:  global
        .offset:         24
        .size:           8
        .value_kind:     global_buffer
      - .offset:         32
        .size:           4
        .value_kind:     hidden_block_count_x
      - .offset:         36
        .size:           4
        .value_kind:     hidden_block_count_y
      - .offset:         40
        .size:           4
        .value_kind:     hidden_block_count_z
      - .offset:         44
        .size:           2
        .value_kind:     hidden_group_size_x
      - .offset:         46
        .size:           2
        .value_kind:     hidden_group_size_y
      - .offset:         48
        .size:           2
        .value_kind:     hidden_group_size_z
      - .offset:         50
        .size:           2
        .value_kind:     hidden_remainder_x
      - .offset:         52
        .size:           2
        .value_kind:     hidden_remainder_y
      - .offset:         54
        .size:           2
        .value_kind:     hidden_remainder_z
      - .offset:         72
        .size:           8
        .value_kind:     hidden_global_offset_x
      - .offset:         80
        .size:           8
        .value_kind:     hidden_global_offset_y
      - .offset:         88
        .size:           8
        .value_kind:     hidden_global_offset_z
      - .offset:         96
        .size:           2
        .value_kind:     hidden_grid_dims
    .group_segment_fixed_size: 0
    .kernarg_segment_align: 8
    .kernarg_segment_size: 288
    .language:       OpenCL C
    .language_version:
      - 2
      - 0
    .max_flat_workgroup_size: 1024
    .name:           _Z13prep_w_kernelPKfS0_S0_PDv8_DF16_
    .private_segment_fixed_size: 0
    .sgpr_count:     18
    .sgpr_spill_count: 0
    .symbol:         _Z13prep_w_kernelPKfS0_S0_PDv8_DF16_.kd
    .uniform_work_group_size: 1
    .uses_dynamic_stack: false
    .vgpr_count:     15
    .vgpr_spill_count: 0
    .wavefront_size: 64
  - .agpr_count:     0
    .args:
      - .actual_access:  read_only
        .address_space:  global
        .offset:         0
        .size:           8
        .value_kind:     global_buffer
      - .actual_access:  read_only
        .address_space:  global
        .offset:         8
        .size:           8
        .value_kind:     global_buffer
      - .actual_access:  write_only
        .address_space:  global
        .offset:         16
        .size:           8
        .value_kind:     global_buffer
      - .actual_access:  write_only
        .address_space:  global
        .offset:         24
        .size:           8
        .value_kind:     global_buffer
      - .actual_access:  write_only
        .address_space:  global
        .offset:         32
        .size:           8
        .value_kind:     global_buffer
    .group_segment_fixed_size: 155904
    .kernarg_segment_align: 8
    .kernarg_segment_size: 40
    .language:       OpenCL C
    .language_version:
      - 2
      - 0
    .max_flat_workgroup_size: 512
    .name:           _Z11proj_kernelPKfPKDv8_DF16_PDF16_S4_S4_
    .private_segment_fixed_size: 0
    .sgpr_count:     26
    .sgpr_spill_count: 0
    .symbol:         _Z11proj_kernelPKfPKDv8_DF16_PDF16_S4_S4_.kd
    .uniform_work_group_size: 1
    .uses_dynamic_stack: false
    .vgpr_count:     176
    .vgpr_spill_count: 0
    .wavefront_size: 64
  - .agpr_count:     0
    .args:
      - .actual_access:  read_only
        .address_space:  global
        .offset:         0
        .size:           8
        .value_kind:     global_buffer
      - .address_space:  global
        .offset:         8
        .size:           8
        .value_kind:     global_buffer
      - .address_space:  global
        .offset:         16
        .size:           8
        .value_kind:     global_buffer
      - .actual_access:  write_only
        .address_space:  global
        .offset:         24
        .size:           8
        .value_kind:     global_buffer
      - .actual_access:  write_only
        .address_space:  global
        .offset:         32
        .size:           8
        .value_kind:     global_buffer
      - .actual_access:  write_only
        .address_space:  global
        .offset:         40
        .size:           8
        .value_kind:     global_buffer
    .group_segment_fixed_size: 65536
    .kernarg_segment_align: 8
    .kernarg_segment_size: 48
    .language:       OpenCL C
    .language_version:
      - 2
      - 0
    .max_flat_workgroup_size: 512
    .name:           _Z11attn_kernelPKDF16_S0_S0_PfPDF16_S1_
    .private_segment_fixed_size: 0
    .sgpr_count:     96
    .sgpr_spill_count: 0
    .symbol:         _Z11attn_kernelPKDF16_S0_S0_PfPDF16_S1_.kd
    .uniform_work_group_size: 1
    .uses_dynamic_stack: false
    .vgpr_count:     122
    .vgpr_spill_count: 0
    .wavefront_size: 64
  - .agpr_count:     0
    .args:
      - .actual_access:  read_only
        .address_space:  global
        .offset:         0
        .size:           8
        .value_kind:     global_buffer
      - .actual_access:  read_only
        .address_space:  global
        .offset:         8
        .size:           8
        .value_kind:     global_buffer
      - .actual_access:  write_only
        .address_space:  global
        .offset:         16
        .size:           8
        .value_kind:     global_buffer
    .group_segment_fixed_size: 0
    .kernarg_segment_align: 8
    .kernarg_segment_size: 24
    .language:       OpenCL C
    .language_version:
      - 2
      - 0
    .max_flat_workgroup_size: 256
    .name:           _Z14combine_kernelPKDF16_PKfPf
    .private_segment_fixed_size: 0
    .sgpr_count:     70
    .sgpr_spill_count: 0
    .symbol:         _Z14combine_kernelPKDF16_PKfPf.kd
    .uniform_work_group_size: 1
    .uses_dynamic_stack: false
    .vgpr_count:     46
    .vgpr_spill_count: 0
    .wavefront_size: 64
